# adaLN prologue: weight rows prefetched 32 rows (8 iterations) ahead in two register sets instead of 4 loads waited per iteration
# speedup vs baseline: 1.0014x; 1.0014x over previous
.LBB0_15:
	s_mul_hi_i32 s4, s14, 0x2aaaaaab
	s_lshr_b32 s5, s4, 31
	s_ashr_i32 s4, s4, 3
	s_add_i32 s4, s4, s5
	s_mul_i32 s5, s4, 48
	s_sub_i32 s5, s14, s5
	v_lshl_or_b32 v6, s5, 7, v18
	s_ashr_i32 s5, s4, 31
	s_lshl_b64 s[6:7], s[4:5], 10
	v_lshl_add_u64 v[8:9], s[6:7], 0, v[2:3]
	v_mad_u64_u32 v[10:11], s[6:7], v8, s8, v[4:5]
	v_mad_i32_i24 v11, v9, s8, v11
	v_ashrrev_i32_e32 v7, 31, v6
	v_lshl_add_u64 v[8:9], v[6:7], 2, v[10:11]
	v_mov_b32_e32 v10, 0
	s_mov_b64 s[6:7], 0
	v_mov_b32_e32 v22, v19
	v_mov_b32_e32 v11, v10
	v_mov_b32_e32 v12, v10
	v_mov_b32_e32 v13, v10
	v_mov_b32_e32 v14, v10
	v_mov_b32_e32 v15, v10
	v_mov_b32_e32 v16, v10
	v_mov_b32_e32 v17, v10
	v_mov_b32_e32 v23, v10
	v_readfirstlane_b32 s100, v8
	v_readfirstlane_b32 s101, v9
	v_and_b32_e32 v200, 63, v0
	v_lshlrev_b32_e32 v200, 2, v200
	s_nop 4
	global_load_dword v70, v200, s[100:101]
	s_add_u32 s100, s100, 0x6000
	s_addc_u32 s101, s101, 0
	global_load_dword v72, v200, s[100:101]
	s_add_u32 s100, s100, 0x6000
	s_addc_u32 s101, s101, 0
	global_load_dword v74, v200, s[100:101]
	s_add_u32 s100, s100, 0x6000
	s_addc_u32 s101, s101, 0
	global_load_dword v76, v200, s[100:101]
	s_add_u32 s100, s100, 0x6000
	s_addc_u32 s101, s101, 0
	global_load_dword v78, v200, s[100:101]
	s_add_u32 s100, s100, 0x6000
	s_addc_u32 s101, s101, 0
	global_load_dword v80, v200, s[100:101]
	s_add_u32 s100, s100, 0x6000
	s_addc_u32 s101, s101, 0
	global_load_dword v82, v200, s[100:101]
	s_add_u32 s100, s100, 0x6000
	s_addc_u32 s101, s101, 0
	global_load_dword v84, v200, s[100:101]
	s_add_u32 s100, s100, 0x6000
	s_addc_u32 s101, s101, 0
	global_load_dword v86, v200, s[100:101]
	s_add_u32 s100, s100, 0x6000
	s_addc_u32 s101, s101, 0
	global_load_dword v88, v200, s[100:101]
	s_add_u32 s100, s100, 0x6000
	s_addc_u32 s101, s101, 0
	global_load_dword v90, v200, s[100:101]
	s_add_u32 s100, s100, 0x6000
	s_addc_u32 s101, s101, 0
	global_load_dword v92, v200, s[100:101]
	s_add_u32 s100, s100, 0x6000
	s_addc_u32 s101, s101, 0
	global_load_dword v94, v200, s[100:101]
	s_add_u32 s100, s100, 0x6000
	s_addc_u32 s101, s101, 0
	global_load_dword v96, v200, s[100:101]
	s_add_u32 s100, s100, 0x6000
	s_addc_u32 s101, s101, 0
	global_load_dword v98, v200, s[100:101]
	s_add_u32 s100, s100, 0x6000
	s_addc_u32 s101, s101, 0
	global_load_dword v100, v200, s[100:101]
	s_add_u32 s100, s100, 0x6000
	s_addc_u32 s101, s101, 0
	global_load_dword v102, v200, s[100:101]
	s_add_u32 s100, s100, 0x6000
	s_addc_u32 s101, s101, 0
	global_load_dword v104, v200, s[100:101]
	s_add_u32 s100, s100, 0x6000
	s_addc_u32 s101, s101, 0
	global_load_dword v106, v200, s[100:101]
	s_add_u32 s100, s100, 0x6000
	s_addc_u32 s101, s101, 0
	global_load_dword v108, v200, s[100:101]
	s_add_u32 s100, s100, 0x6000
	s_addc_u32 s101, s101, 0
	global_load_dword v110, v200, s[100:101]
	s_add_u32 s100, s100, 0x6000
	s_addc_u32 s101, s101, 0
	global_load_dword v112, v200, s[100:101]
	s_add_u32 s100, s100, 0x6000
	s_addc_u32 s101, s101, 0
	global_load_dword v114, v200, s[100:101]
	s_add_u32 s100, s100, 0x6000
	s_addc_u32 s101, s101, 0
	global_load_dword v116, v200, s[100:101]
	s_add_u32 s100, s100, 0x6000
	s_addc_u32 s101, s101, 0
	global_load_dword v118, v200, s[100:101]
	s_add_u32 s100, s100, 0x6000
	s_addc_u32 s101, s101, 0
	global_load_dword v120, v200, s[100:101]
	s_add_u32 s100, s100, 0x6000
	s_addc_u32 s101, s101, 0
	global_load_dword v122, v200, s[100:101]
	s_add_u32 s100, s100, 0x6000
	s_addc_u32 s101, s101, 0
	global_load_dword v124, v200, s[100:101]
	s_add_u32 s100, s100, 0x6000
	s_addc_u32 s101, s101, 0
	global_load_dword v126, v200, s[100:101]
	s_add_u32 s100, s100, 0x6000
	s_addc_u32 s101, s101, 0
	global_load_dword v128, v200, s[100:101]
	s_add_u32 s100, s100, 0x6000
	s_addc_u32 s101, s101, 0
	global_load_dword v130, v200, s[100:101]
	s_add_u32 s100, s100, 0x6000
	s_addc_u32 s101, s101, 0
	global_load_dword v132, v200, s[100:101]
	s_add_u32 s100, s100, 0x6000
	s_addc_u32 s101, s101, 0
	s_mov_b32 s6, 0
.Lada_loop:
	global_load_dword v134, v200, s[100:101]
	s_add_u32 s100, s100, 0x6000
	s_addc_u32 s101, s101, 0
	global_load_dword v136, v200, s[100:101]
	s_add_u32 s100, s100, 0x6000
	s_addc_u32 s101, s101, 0
	global_load_dword v138, v200, s[100:101]
	s_add_u32 s100, s100, 0x6000
	s_addc_u32 s101, s101, 0
	global_load_dword v140, v200, s[100:101]
	s_add_u32 s100, s100, 0x6000
	s_addc_u32 s101, s101, 0
	global_load_dword v142, v200, s[100:101]
	s_add_u32 s100, s100, 0x6000
	s_addc_u32 s101, s101, 0
	global_load_dword v144, v200, s[100:101]
	s_add_u32 s100, s100, 0x6000
	s_addc_u32 s101, s101, 0
	global_load_dword v146, v200, s[100:101]
	s_add_u32 s100, s100, 0x6000
	s_addc_u32 s101, s101, 0
	global_load_dword v148, v200, s[100:101]
	s_add_u32 s100, s100, 0x6000
	s_addc_u32 s101, s101, 0
	global_load_dword v150, v200, s[100:101]
	s_add_u32 s100, s100, 0x6000
	s_addc_u32 s101, s101, 0
	global_load_dword v152, v200, s[100:101]
	s_add_u32 s100, s100, 0x6000
	s_addc_u32 s101, s101, 0
	global_load_dword v154, v200, s[100:101]
	s_add_u32 s100, s100, 0x6000
	s_addc_u32 s101, s101, 0
	global_load_dword v156, v200, s[100:101]
	s_add_u32 s100, s100, 0x6000
	s_addc_u32 s101, s101, 0
	global_load_dword v158, v200, s[100:101]
	s_add_u32 s100, s100, 0x6000
	s_addc_u32 s101, s101, 0
	global_load_dword v160, v200, s[100:101]
	s_add_u32 s100, s100, 0x6000
	s_addc_u32 s101, s101, 0
	global_load_dword v162, v200, s[100:101]
	s_add_u32 s100, s100, 0x6000
	s_addc_u32 s101, s101, 0
	global_load_dword v164, v200, s[100:101]
	s_add_u32 s100, s100, 0x6000
	s_addc_u32 s101, s101, 0
	global_load_dword v166, v200, s[100:101]
	s_add_u32 s100, s100, 0x6000
	s_addc_u32 s101, s101, 0
	global_load_dword v168, v200, s[100:101]
	s_add_u32 s100, s100, 0x6000
	s_addc_u32 s101, s101, 0
	global_load_dword v170, v200, s[100:101]
	s_add_u32 s100, s100, 0x6000
	s_addc_u32 s101, s101, 0
	global_load_dword v172, v200, s[100:101]
	s_add_u32 s100, s100, 0x6000
	s_addc_u32 s101, s101, 0
	global_load_dword v174, v200, s[100:101]
	s_add_u32 s100, s100, 0x6000
	s_addc_u32 s101, s101, 0
	global_load_dword v176, v200, s[100:101]
	s_add_u32 s100, s100, 0x6000
	s_addc_u32 s101, s101, 0
	global_load_dword v178, v200, s[100:101]
	s_add_u32 s100, s100, 0x6000
	s_addc_u32 s101, s101, 0
	global_load_dword v180, v200, s[100:101]
	s_add_u32 s100, s100, 0x6000
	s_addc_u32 s101, s101, 0
	global_load_dword v182, v200, s[100:101]
	s_add_u32 s100, s100, 0x6000
	s_addc_u32 s101, s101, 0
	global_load_dword v184, v200, s[100:101]
	s_add_u32 s100, s100, 0x6000
	s_addc_u32 s101, s101, 0
	global_load_dword v186, v200, s[100:101]
	s_add_u32 s100, s100, 0x6000
	s_addc_u32 s101, s101, 0
	global_load_dword v188, v200, s[100:101]
	s_add_u32 s100, s100, 0x6000
	s_addc_u32 s101, s101, 0
	global_load_dword v190, v200, s[100:101]
	s_add_u32 s100, s100, 0x6000
	s_addc_u32 s101, s101, 0
	global_load_dword v192, v200, s[100:101]
	s_add_u32 s100, s100, 0x6000
	s_addc_u32 s101, s101, 0
	global_load_dword v194, v200, s[100:101]
	s_add_u32 s100, s100, 0x6000
	s_addc_u32 s101, s101, 0
	global_load_dword v196, v200, s[100:101]
	s_add_u32 s100, s100, 0x6000
	s_addc_u32 s101, s101, 0
	ds_read_b128 v[24:27], v22 offset:4096
	ds_read_b128 v[28:31], v22 offset:8192
	ds_read_b128 v[32:35], v22 offset:12288
	ds_read_b128 v[36:39], v22 offset:16384
	ds_read_b128 v[40:43], v22 offset:20480
	ds_read_b128 v[44:47], v22 offset:24576
	ds_read_b128 v[48:51], v22 offset:28672
	ds_read_b128 v[52:55], v22
	ds_read_b128 v[56:59], v22 offset:32768
	s_waitcnt lgkmcnt(8)
	v_mov_b32_e32 v69, v24
	v_add_u32_e32 v22, 16, v22
	s_waitcnt lgkmcnt(1)
	v_mov_b32_e32 v68, v52
	v_mov_b32_e32 v24, v53
	v_mov_b32_e32 v52, v54
	v_mov_b32_e32 v53, v26
	v_mov_b32_e32 v26, v55
	v_mov_b32_e32 v54, v28
	v_mov_b32_e32 v55, v32
	v_mov_b32_e32 v32, v29
	v_mov_b32_e32 v28, v30
	v_mov_b32_e32 v29, v34
	v_mov_b32_e32 v34, v31
	v_mov_b32_e32 v30, v36
	v_mov_b32_e32 v31, v40
	v_mov_b32_e32 v40, v37
	v_mov_b32_e32 v36, v38
	v_mov_b32_e32 v37, v42
	v_mov_b32_e32 v42, v39
	v_mov_b32_e32 v38, v44
	v_mov_b32_e32 v39, v48
	v_mov_b32_e32 v48, v45
	v_mov_b32_e32 v44, v46
	v_mov_b32_e32 v45, v50
	v_mov_b32_e32 v50, v47
	s_waitcnt vmcnt(60)
	v_pk_fma_f32 v[10:11], v[70:71], v[68:69], v[10:11] op_sel_hi:[0,1,1]
	v_pk_fma_f32 v[12:13], v[70:71], v[54:55], v[12:13] op_sel_hi:[0,1,1]
	v_pk_fma_f32 v[14:15], v[70:71], v[30:31], v[14:15] op_sel_hi:[0,1,1]
	v_pk_fma_f32 v[16:17], v[70:71], v[38:39], v[16:17] op_sel_hi:[0,1,1]
	s_waitcnt lgkmcnt(0)
	v_fmac_f32_e32 v23, v70, v56
	v_pk_fma_f32 v[10:11], v[72:73], v[24:25], v[10:11] op_sel_hi:[0,1,1]
	v_pk_fma_f32 v[12:13], v[72:73], v[32:33], v[12:13] op_sel_hi:[0,1,1]
	v_pk_fma_f32 v[14:15], v[72:73], v[40:41], v[14:15] op_sel_hi:[0,1,1]
	v_pk_fma_f32 v[16:17], v[72:73], v[48:49], v[16:17] op_sel_hi:[0,1,1]
	v_fmac_f32_e32 v23, v72, v57
	v_pk_fma_f32 v[10:11], v[74:75], v[52:53], v[10:11] op_sel_hi:[0,1,1]
	v_pk_fma_f32 v[12:13], v[74:75], v[28:29], v[12:13] op_sel_hi:[0,1,1]
	v_pk_fma_f32 v[14:15], v[74:75], v[36:37], v[14:15] op_sel_hi:[0,1,1]
	v_pk_fma_f32 v[16:17], v[74:75], v[44:45], v[16:17] op_sel_hi:[0,1,1]
	v_fmac_f32_e32 v23, v74, v58
	v_pk_fma_f32 v[10:11], v[76:77], v[26:27], v[10:11] op_sel_hi:[0,1,1]
	v_pk_fma_f32 v[12:13], v[76:77], v[34:35], v[12:13] op_sel_hi:[0,1,1]
	v_pk_fma_f32 v[14:15], v[76:77], v[42:43], v[14:15] op_sel_hi:[0,1,1]
	v_pk_fma_f32 v[16:17], v[76:77], v[50:51], v[16:17] op_sel_hi:[0,1,1]
	v_fmac_f32_e32 v23, v76, v59
	ds_read_b128 v[24:27], v22 offset:4096
	ds_read_b128 v[28:31], v22 offset:8192
	ds_read_b128 v[32:35], v22 offset:12288
	ds_read_b128 v[36:39], v22 offset:16384
	ds_read_b128 v[40:43], v22 offset:20480
	ds_read_b128 v[44:47], v22 offset:24576
	ds_read_b128 v[48:51], v22 offset:28672
	ds_read_b128 v[52:55], v22
	ds_read_b128 v[56:59], v22 offset:32768
	s_waitcnt lgkmcnt(8)
	v_mov_b32_e32 v69, v24
	v_add_u32_e32 v22, 16, v22
	s_waitcnt lgkmcnt(1)
	v_mov_b32_e32 v68, v52
	v_mov_b32_e32 v24, v53
	v_mov_b32_e32 v52, v54
	v_mov_b32_e32 v53, v26
	v_mov_b32_e32 v26, v55
	v_mov_b32_e32 v54, v28
	v_mov_b32_e32 v55, v32
	v_mov_b32_e32 v32, v29
	v_mov_b32_e32 v28, v30
	v_mov_b32_e32 v29, v34
	v_mov_b32_e32 v34, v31
	v_mov_b32_e32 v30, v36
	v_mov_b32_e32 v31, v40
	v_mov_b32_e32 v40, v37
	v_mov_b32_e32 v36, v38
	v_mov_b32_e32 v37, v42
	v_mov_b32_e32 v42, v39
	v_mov_b32_e32 v38, v44
	v_mov_b32_e32 v39, v48
	v_mov_b32_e32 v48, v45
	v_mov_b32_e32 v44, v46
	v_mov_b32_e32 v45, v50
	v_mov_b32_e32 v50, v47
	s_waitcnt vmcnt(56)
	v_pk_fma_f32 v[10:11], v[78:79], v[68:69], v[10:11] op_sel_hi:[0,1,1]
	v_pk_fma_f32 v[12:13], v[78:79], v[54:55], v[12:13] op_sel_hi:[0,1,1]
	v_pk_fma_f32 v[14:15], v[78:79], v[30:31], v[14:15] op_sel_hi:[0,1,1]
	v_pk_fma_f32 v[16:17], v[78:79], v[38:39], v[16:17] op_sel_hi:[0,1,1]
	s_waitcnt lgkmcnt(0)
	v_fmac_f32_e32 v23, v78, v56
	v_pk_fma_f32 v[10:11], v[80:81], v[24:25], v[10:11] op_sel_hi:[0,1,1]
	v_pk_fma_f32 v[12:13], v[80:81], v[32:33], v[12:13] op_sel_hi:[0,1,1]
	v_pk_fma_f32 v[14:15], v[80:81], v[40:41], v[14:15] op_sel_hi:[0,1,1]
	v_pk_fma_f32 v[16:17], v[80:81], v[48:49], v[16:17] op_sel_hi:[0,1,1]
	v_fmac_f32_e32 v23, v80, v57
	v_pk_fma_f32 v[10:11], v[82:83], v[52:53], v[10:11] op_sel_hi:[0,1,1]
	v_pk_fma_f32 v[12:13], v[82:83], v[28:29], v[12:13] op_sel_hi:[0,1,1]
	v_pk_fma_f32 v[14:15], v[82:83], v[36:37], v[14:15] op_sel_hi:[0,1,1]
	v_pk_fma_f32 v[16:17], v[82:83], v[44:45], v[16:17] op_sel_hi:[0,1,1]
	v_fmac_f32_e32 v23, v82, v58
	v_pk_fma_f32 v[10:11], v[84:85], v[26:27], v[10:11] op_sel_hi:[0,1,1]
	v_pk_fma_f32 v[12:13], v[84:85], v[34:35], v[12:13] op_sel_hi:[0,1,1]
	v_pk_fma_f32 v[14:15], v[84:85], v[42:43], v[14:15] op_sel_hi:[0,1,1]
	v_pk_fma_f32 v[16:17], v[84:85], v[50:51], v[16:17] op_sel_hi:[0,1,1]
	v_fmac_f32_e32 v23, v84, v59
	ds_read_b128 v[24:27], v22 offset:4096
	ds_read_b128 v[28:31], v22 offset:8192
	ds_read_b128 v[32:35], v22 offset:12288
	ds_read_b128 v[36:39], v22 offset:16384
	ds_read_b128 v[40:43], v22 offset:20480
	ds_read_b128 v[44:47], v22 offset:24576
	ds_read_b128 v[48:51], v22 offset:28672
	ds_read_b128 v[52:55], v22
	ds_read_b128 v[56:59], v22 offset:32768
	s_waitcnt lgkmcnt(8)
	v_mov_b32_e32 v69, v24
	v_add_u32_e32 v22, 16, v22
	s_waitcnt lgkmcnt(1)
	v_mov_b32_e32 v68, v52
	v_mov_b32_e32 v24, v53
	v_mov_b32_e32 v52, v54
	v_mov_b32_e32 v53, v26
	v_mov_b32_e32 v26, v55
	v_mov_b32_e32 v54, v28
	v_mov_b32_e32 v55, v32
	v_mov_b32_e32 v32, v29
	v_mov_b32_e32 v28, v30
	v_mov_b32_e32 v29, v34
	v_mov_b32_e32 v34, v31
	v_mov_b32_e32 v30, v36
	v_mov_b32_e32 v31, v40
	v_mov_b32_e32 v40, v37
	v_mov_b32_e32 v36, v38
	v_mov_b32_e32 v37, v42
	v_mov_b32_e32 v42, v39
	v_mov_b32_e32 v38, v44
	v_mov_b32_e32 v39, v48
	v_mov_b32_e32 v48, v45
	v_mov_b32_e32 v44, v46
	v_mov_b32_e32 v45, v50
	v_mov_b32_e32 v50, v47
	s_waitcnt vmcnt(52)
	v_pk_fma_f32 v[10:11], v[86:87], v[68:69], v[10:11] op_sel_hi:[0,1,1]
	v_pk_fma_f32 v[12:13], v[86:87], v[54:55], v[12:13] op_sel_hi:[0,1,1]
	v_pk_fma_f32 v[14:15], v[86:87], v[30:31], v[14:15] op_sel_hi:[0,1,1]
	v_pk_fma_f32 v[16:17], v[86:87], v[38:39], v[16:17] op_sel_hi:[0,1,1]
	s_waitcnt lgkmcnt(0)
	v_fmac_f32_e32 v23, v86, v56
	v_pk_fma_f32 v[10:11], v[88:89], v[24:25], v[10:11] op_sel_hi:[0,1,1]
	v_pk_fma_f32 v[12:13], v[88:89], v[32:33], v[12:13] op_sel_hi:[0,1,1]
	v_pk_fma_f32 v[14:15], v[88:89], v[40:41], v[14:15] op_sel_hi:[0,1,1]
	v_pk_fma_f32 v[16:17], v[88:89], v[48:49], v[16:17] op_sel_hi:[0,1,1]
	v_fmac_f32_e32 v23, v88, v57
	v_pk_fma_f32 v[10:11], v[90:91], v[52:53], v[10:11] op_sel_hi:[0,1,1]
	v_pk_fma_f32 v[12:13], v[90:91], v[28:29], v[12:13] op_sel_hi:[0,1,1]
	v_pk_fma_f32 v[14:15], v[90:91], v[36:37], v[14:15] op_sel_hi:[0,1,1]
	v_pk_fma_f32 v[16:17], v[90:91], v[44:45], v[16:17] op_sel_hi:[0,1,1]
	v_fmac_f32_e32 v23, v90, v58
	v_pk_fma_f32 v[10:11], v[92:93], v[26:27], v[10:11] op_sel_hi:[0,1,1]
	v_pk_fma_f32 v[12:13], v[92:93], v[34:35], v[12:13] op_sel_hi:[0,1,1]
	v_pk_fma_f32 v[14:15], v[92:93], v[42:43], v[14:15] op_sel_hi:[0,1,1]
	v_pk_fma_f32 v[16:17], v[92:93], v[50:51], v[16:17] op_sel_hi:[0,1,1]
	v_fmac_f32_e32 v23, v92, v59
	ds_read_b128 v[24:27], v22 offset:4096
	ds_read_b128 v[28:31], v22 offset:8192
	ds_read_b128 v[32:35], v22 offset:12288
	ds_read_b128 v[36:39], v22 offset:16384
	ds_read_b128 v[40:43], v22 offset:20480
	ds_read_b128 v[44:47], v22 offset:24576
	ds_read_b128 v[48:51], v22 offset:28672
	ds_read_b128 v[52:55], v22
	ds_read_b128 v[56:59], v22 offset:32768
	s_waitcnt lgkmcnt(8)
	v_mov_b32_e32 v69, v24
	v_add_u32_e32 v22, 16, v22
	s_waitcnt lgkmcnt(1)
	v_mov_b32_e32 v68, v52
	v_mov_b32_e32 v24, v53
	v_mov_b32_e32 v52, v54
	v_mov_b32_e32 v53, v26
	v_mov_b32_e32 v26, v55
	v_mov_b32_e32 v54, v28
	v_mov_b32_e32 v55, v32
	v_mov_b32_e32 v32, v29
	v_mov_b32_e32 v28, v30
	v_mov_b32_e32 v29, v34
	v_mov_b32_e32 v34, v31
	v_mov_b32_e32 v30, v36
	v_mov_b32_e32 v31, v40
	v_mov_b32_e32 v40, v37
	v_mov_b32_e32 v36, v38
	v_mov_b32_e32 v37, v42
	v_mov_b32_e32 v42, v39
	v_mov_b32_e32 v38, v44
	v_mov_b32_e32 v39, v48
	v_mov_b32_e32 v48, v45
	v_mov_b32_e32 v44, v46
	v_mov_b32_e32 v45, v50
	v_mov_b32_e32 v50, v47
	s_waitcnt vmcnt(48)
	v_pk_fma_f32 v[10:11], v[94:95], v[68:69], v[10:11] op_sel_hi:[0,1,1]
	v_pk_fma_f32 v[12:13], v[94:95], v[54:55], v[12:13] op_sel_hi:[0,1,1]
	v_pk_fma_f32 v[14:15], v[94:95], v[30:31], v[14:15] op_sel_hi:[0,1,1]
	v_pk_fma_f32 v[16:17], v[94:95], v[38:39], v[16:17] op_sel_hi:[0,1,1]
	s_waitcnt lgkmcnt(0)
	v_fmac_f32_e32 v23, v94, v56
	v_pk_fma_f32 v[10:11], v[96:97], v[24:25], v[10:11] op_sel_hi:[0,1,1]
	v_pk_fma_f32 v[12:13], v[96:97], v[32:33], v[12:13] op_sel_hi:[0,1,1]
	v_pk_fma_f32 v[14:15], v[96:97], v[40:41], v[14:15] op_sel_hi:[0,1,1]
	v_pk_fma_f32 v[16:17], v[96:97], v[48:49], v[16:17] op_sel_hi:[0,1,1]
	v_fmac_f32_e32 v23, v96, v57
	v_pk_fma_f32 v[10:11], v[98:99], v[52:53], v[10:11] op_sel_hi:[0,1,1]
	v_pk_fma_f32 v[12:13], v[98:99], v[28:29], v[12:13] op_sel_hi:[0,1,1]
	v_pk_fma_f32 v[14:15], v[98:99], v[36:37], v[14:15] op_sel_hi:[0,1,1]
	v_pk_fma_f32 v[16:17], v[98:99], v[44:45], v[16:17] op_sel_hi:[0,1,1]
	v_fmac_f32_e32 v23, v98, v58
	v_pk_fma_f32 v[10:11], v[100:101], v[26:27], v[10:11] op_sel_hi:[0,1,1]
	v_pk_fma_f32 v[12:13], v[100:101], v[34:35], v[12:13] op_sel_hi:[0,1,1]
	v_pk_fma_f32 v[14:15], v[100:101], v[42:43], v[14:15] op_sel_hi:[0,1,1]
	v_pk_fma_f32 v[16:17], v[100:101], v[50:51], v[16:17] op_sel_hi:[0,1,1]
	v_fmac_f32_e32 v23, v100, v59
	ds_read_b128 v[24:27], v22 offset:4096
	ds_read_b128 v[28:31], v22 offset:8192
	ds_read_b128 v[32:35], v22 offset:12288
	ds_read_b128 v[36:39], v22 offset:16384
	ds_read_b128 v[40:43], v22 offset:20480
	ds_read_b128 v[44:47], v22 offset:24576
	ds_read_b128 v[48:51], v22 offset:28672
	ds_read_b128 v[52:55], v22
	ds_read_b128 v[56:59], v22 offset:32768
	s_waitcnt lgkmcnt(8)
	v_mov_b32_e32 v69, v24
	v_add_u32_e32 v22, 16, v22
	s_waitcnt lgkmcnt(1)
	v_mov_b32_e32 v68, v52
	v_mov_b32_e32 v24, v53
	v_mov_b32_e32 v52, v54
	v_mov_b32_e32 v53, v26
	v_mov_b32_e32 v26, v55
	v_mov_b32_e32 v54, v28
	v_mov_b32_e32 v55, v32
	v_mov_b32_e32 v32, v29
	v_mov_b32_e32 v28, v30
	v_mov_b32_e32 v29, v34
	v_mov_b32_e32 v34, v31
	v_mov_b32_e32 v30, v36
	v_mov_b32_e32 v31, v40
	v_mov_b32_e32 v40, v37
	v_mov_b32_e32 v36, v38
	v_mov_b32_e32 v37, v42
	v_mov_b32_e32 v42, v39
	v_mov_b32_e32 v38, v44
	v_mov_b32_e32 v39, v48
	v_mov_b32_e32 v48, v45
	v_mov_b32_e32 v44, v46
	v_mov_b32_e32 v45, v50
	v_mov_b32_e32 v50, v47
	s_waitcnt vmcnt(44)
	v_pk_fma_f32 v[10:11], v[102:103], v[68:69], v[10:11] op_sel_hi:[0,1,1]
	v_pk_fma_f32 v[12:13], v[102:103], v[54:55], v[12:13] op_sel_hi:[0,1,1]
	v_pk_fma_f32 v[14:15], v[102:103], v[30:31], v[14:15] op_sel_hi:[0,1,1]
	v_pk_fma_f32 v[16:17], v[102:103], v[38:39], v[16:17] op_sel_hi:[0,1,1]
	s_waitcnt lgkmcnt(0)
	v_fmac_f32_e32 v23, v102, v56
	v_pk_fma_f32 v[10:11], v[104:105], v[24:25], v[10:11] op_sel_hi:[0,1,1]
	v_pk_fma_f32 v[12:13], v[104:105], v[32:33], v[12:13] op_sel_hi:[0,1,1]
	v_pk_fma_f32 v[14:15], v[104:105], v[40:41], v[14:15] op_sel_hi:[0,1,1]
	v_pk_fma_f32 v[16:17], v[104:105], v[48:49], v[16:17] op_sel_hi:[0,1,1]
	v_fmac_f32_e32 v23, v104, v57
	v_pk_fma_f32 v[10:11], v[106:107], v[52:53], v[10:11] op_sel_hi:[0,1,1]
	v_pk_fma_f32 v[12:13], v[106:107], v[28:29], v[12:13] op_sel_hi:[0,1,1]
	v_pk_fma_f32 v[14:15], v[106:107], v[36:37], v[14:15] op_sel_hi:[0,1,1]
	v_pk_fma_f32 v[16:17], v[106:107], v[44:45], v[16:17] op_sel_hi:[0,1,1]
	v_fmac_f32_e32 v23, v106, v58
	v_pk_fma_f32 v[10:11], v[108:109], v[26:27], v[10:11] op_sel_hi:[0,1,1]
	v_pk_fma_f32 v[12:13], v[108:109], v[34:35], v[12:13] op_sel_hi:[0,1,1]
	v_pk_fma_f32 v[14:15], v[108:109], v[42:43], v[14:15] op_sel_hi:[0,1,1]
	v_pk_fma_f32 v[16:17], v[108:109], v[50:51], v[16:17] op_sel_hi:[0,1,1]
	v_fmac_f32_e32 v23, v108, v59
	ds_read_b128 v[24:27], v22 offset:4096
	ds_read_b128 v[28:31], v22 offset:8192
	ds_read_b128 v[32:35], v22 offset:12288
	ds_read_b128 v[36:39], v22 offset:16384
	ds_read_b128 v[40:43], v22 offset:20480
	ds_read_b128 v[44:47], v22 offset:24576
	ds_read_b128 v[48:51], v22 offset:28672
	ds_read_b128 v[52:55], v22
	ds_read_b128 v[56:59], v22 offset:32768
	s_waitcnt lgkmcnt(8)
	v_mov_b32_e32 v69, v24
	v_add_u32_e32 v22, 16, v22
	s_waitcnt lgkmcnt(1)
	v_mov_b32_e32 v68, v52
	v_mov_b32_e32 v24, v53
	v_mov_b32_e32 v52, v54
	v_mov_b32_e32 v53, v26
	v_mov_b32_e32 v26, v55
	v_mov_b32_e32 v54, v28
	v_mov_b32_e32 v55, v32
	v_mov_b32_e32 v32, v29
	v_mov_b32_e32 v28, v30
	v_mov_b32_e32 v29, v34
	v_mov_b32_e32 v34, v31
	v_mov_b32_e32 v30, v36
	v_mov_b32_e32 v31, v40
	v_mov_b32_e32 v40, v37
	v_mov_b32_e32 v36, v38
	v_mov_b32_e32 v37, v42
	v_mov_b32_e32 v42, v39
	v_mov_b32_e32 v38, v44
	v_mov_b32_e32 v39, v48
	v_mov_b32_e32 v48, v45
	v_mov_b32_e32 v44, v46
	v_mov_b32_e32 v45, v50
	v_mov_b32_e32 v50, v47
	s_waitcnt vmcnt(40)
	v_pk_fma_f32 v[10:11], v[110:111], v[68:69], v[10:11] op_sel_hi:[0,1,1]
	v_pk_fma_f32 v[12:13], v[110:111], v[54:55], v[12:13] op_sel_hi:[0,1,1]
	v_pk_fma_f32 v[14:15], v[110:111], v[30:31], v[14:15] op_sel_hi:[0,1,1]
	v_pk_fma_f32 v[16:17], v[110:111], v[38:39], v[16:17] op_sel_hi:[0,1,1]
	s_waitcnt lgkmcnt(0)
	v_fmac_f32_e32 v23, v110, v56
	v_pk_fma_f32 v[10:11], v[112:113], v[24:25], v[10:11] op_sel_hi:[0,1,1]
	v_pk_fma_f32 v[12:13], v[112:113], v[32:33], v[12:13] op_sel_hi:[0,1,1]
	v_pk_fma_f32 v[14:15], v[112:113], v[40:41], v[14:15] op_sel_hi:[0,1,1]
	v_pk_fma_f32 v[16:17], v[112:113], v[48:49], v[16:17] op_sel_hi:[0,1,1]
	v_fmac_f32_e32 v23, v112, v57
	v_pk_fma_f32 v[10:11], v[114:115], v[52:53], v[10:11] op_sel_hi:[0,1,1]
	v_pk_fma_f32 v[12:13], v[114:115], v[28:29], v[12:13] op_sel_hi:[0,1,1]
	v_pk_fma_f32 v[14:15], v[114:115], v[36:37], v[14:15] op_sel_hi:[0,1,1]
	v_pk_fma_f32 v[16:17], v[114:115], v[44:45], v[16:17] op_sel_hi:[0,1,1]
	v_fmac_f32_e32 v23, v114, v58
	v_pk_fma_f32 v[10:11], v[116:117], v[26:27], v[10:11] op_sel_hi:[0,1,1]
	v_pk_fma_f32 v[12:13], v[116:117], v[34:35], v[12:13] op_sel_hi:[0,1,1]
	v_pk_fma_f32 v[14:15], v[116:117], v[42:43], v[14:15] op_sel_hi:[0,1,1]
	v_pk_fma_f32 v[16:17], v[116:117], v[50:51], v[16:17] op_sel_hi:[0,1,1]
	v_fmac_f32_e32 v23, v116, v59
	ds_read_b128 v[24:27], v22 offset:4096
	ds_read_b128 v[28:31], v22 offset:8192
	ds_read_b128 v[32:35], v22 offset:12288
	ds_read_b128 v[36:39], v22 offset:16384
	ds_read_b128 v[40:43], v22 offset:20480
	ds_read_b128 v[44:47], v22 offset:24576
	ds_read_b128 v[48:51], v22 offset:28672
	ds_read_b128 v[52:55], v22
	ds_read_b128 v[56:59], v22 offset:32768
	s_waitcnt lgkmcnt(8)
	v_mov_b32_e32 v69, v24
	v_add_u32_e32 v22, 16, v22
	s_waitcnt lgkmcnt(1)
	v_mov_b32_e32 v68, v52
	v_mov_b32_e32 v24, v53
	v_mov_b32_e32 v52, v54
	v_mov_b32_e32 v53, v26
	v_mov_b32_e32 v26, v55
	v_mov_b32_e32 v54, v28
	v_mov_b32_e32 v55, v32
	v_mov_b32_e32 v32, v29
	v_mov_b32_e32 v28, v30
	v_mov_b32_e32 v29, v34
	v_mov_b32_e32 v34, v31
	v_mov_b32_e32 v30, v36
	v_mov_b32_e32 v31, v40
	v_mov_b32_e32 v40, v37
	v_mov_b32_e32 v36, v38
	v_mov_b32_e32 v37, v42
	v_mov_b32_e32 v42, v39
	v_mov_b32_e32 v38, v44
	v_mov_b32_e32 v39, v48
	v_mov_b32_e32 v48, v45
	v_mov_b32_e32 v44, v46
	v_mov_b32_e32 v45, v50
	v_mov_b32_e32 v50, v47
	s_waitcnt vmcnt(36)
	v_pk_fma_f32 v[10:11], v[118:119], v[68:69], v[10:11] op_sel_hi:[0,1,1]
	v_pk_fma_f32 v[12:13], v[118:119], v[54:55], v[12:13] op_sel_hi:[0,1,1]
	v_pk_fma_f32 v[14:15], v[118:119], v[30:31], v[14:15] op_sel_hi:[0,1,1]
	v_pk_fma_f32 v[16:17], v[118:119], v[38:39], v[16:17] op_sel_hi:[0,1,1]
	s_waitcnt lgkmcnt(0)
	v_fmac_f32_e32 v23, v118, v56
	v_pk_fma_f32 v[10:11], v[120:121], v[24:25], v[10:11] op_sel_hi:[0,1,1]
	v_pk_fma_f32 v[12:13], v[120:121], v[32:33], v[12:13] op_sel_hi:[0,1,1]
	v_pk_fma_f32 v[14:15], v[120:121], v[40:41], v[14:15] op_sel_hi:[0,1,1]
	v_pk_fma_f32 v[16:17], v[120:121], v[48:49], v[16:17] op_sel_hi:[0,1,1]
	v_fmac_f32_e32 v23, v120, v57
	v_pk_fma_f32 v[10:11], v[122:123], v[52:53], v[10:11] op_sel_hi:[0,1,1]
	v_pk_fma_f32 v[12:13], v[122:123], v[28:29], v[12:13] op_sel_hi:[0,1,1]
	v_pk_fma_f32 v[14:15], v[122:123], v[36:37], v[14:15] op_sel_hi:[0,1,1]
	v_pk_fma_f32 v[16:17], v[122:123], v[44:45], v[16:17] op_sel_hi:[0,1,1]
	v_fmac_f32_e32 v23, v122, v58
	v_pk_fma_f32 v[10:11], v[124:125], v[26:27], v[10:11] op_sel_hi:[0,1,1]
	v_pk_fma_f32 v[12:13], v[124:125], v[34:35], v[12:13] op_sel_hi:[0,1,1]
	v_pk_fma_f32 v[14:15], v[124:125], v[42:43], v[14:15] op_sel_hi:[0,1,1]
	v_pk_fma_f32 v[16:17], v[124:125], v[50:51], v[16:17] op_sel_hi:[0,1,1]
	v_fmac_f32_e32 v23, v124, v59
	ds_read_b128 v[24:27], v22 offset:4096
	ds_read_b128 v[28:31], v22 offset:8192
	ds_read_b128 v[32:35], v22 offset:12288
	ds_read_b128 v[36:39], v22 offset:16384
	ds_read_b128 v[40:43], v22 offset:20480
	ds_read_b128 v[44:47], v22 offset:24576
	ds_read_b128 v[48:51], v22 offset:28672
	ds_read_b128 v[52:55], v22
	ds_read_b128 v[56:59], v22 offset:32768
	s_waitcnt lgkmcnt(8)
	v_mov_b32_e32 v69, v24
	v_add_u32_e32 v22, 16, v22
	s_waitcnt lgkmcnt(1)
	v_mov_b32_e32 v68, v52
	v_mov_b32_e32 v24, v53
	v_mov_b32_e32 v52, v54
	v_mov_b32_e32 v53, v26
	v_mov_b32_e32 v26, v55
	v_mov_b32_e32 v54, v28
	v_mov_b32_e32 v55, v32
	v_mov_b32_e32 v32, v29
	v_mov_b32_e32 v28, v30
	v_mov_b32_e32 v29, v34
	v_mov_b32_e32 v34, v31
	v_mov_b32_e32 v30, v36
	v_mov_b32_e32 v31, v40
	v_mov_b32_e32 v40, v37
	v_mov_b32_e32 v36, v38
	v_mov_b32_e32 v37, v42
	v_mov_b32_e32 v42, v39
	v_mov_b32_e32 v38, v44
	v_mov_b32_e32 v39, v48
	v_mov_b32_e32 v48, v45
	v_mov_b32_e32 v44, v46
	v_mov_b32_e32 v45, v50
	v_mov_b32_e32 v50, v47
	s_waitcnt vmcnt(32)
	v_pk_fma_f32 v[10:11], v[126:127], v[68:69], v[10:11] op_sel_hi:[0,1,1]
	v_pk_fma_f32 v[12:13], v[126:127], v[54:55], v[12:13] op_sel_hi:[0,1,1]
	v_pk_fma_f32 v[14:15], v[126:127], v[30:31], v[14:15] op_sel_hi:[0,1,1]
	v_pk_fma_f32 v[16:17], v[126:127], v[38:39], v[16:17] op_sel_hi:[0,1,1]
	s_waitcnt lgkmcnt(0)
	v_fmac_f32_e32 v23, v126, v56
	v_pk_fma_f32 v[10:11], v[128:129], v[24:25], v[10:11] op_sel_hi:[0,1,1]
	v_pk_fma_f32 v[12:13], v[128:129], v[32:33], v[12:13] op_sel_hi:[0,1,1]
	v_pk_fma_f32 v[14:15], v[128:129], v[40:41], v[14:15] op_sel_hi:[0,1,1]
	v_pk_fma_f32 v[16:17], v[128:129], v[48:49], v[16:17] op_sel_hi:[0,1,1]
	v_fmac_f32_e32 v23, v128, v57
	v_pk_fma_f32 v[10:11], v[130:131], v[52:53], v[10:11] op_sel_hi:[0,1,1]
	v_pk_fma_f32 v[12:13], v[130:131], v[28:29], v[12:13] op_sel_hi:[0,1,1]
	v_pk_fma_f32 v[14:15], v[130:131], v[36:37], v[14:15] op_sel_hi:[0,1,1]
	v_pk_fma_f32 v[16:17], v[130:131], v[44:45], v[16:17] op_sel_hi:[0,1,1]
	v_fmac_f32_e32 v23, v130, v58
	v_pk_fma_f32 v[10:11], v[132:133], v[26:27], v[10:11] op_sel_hi:[0,1,1]
	v_pk_fma_f32 v[12:13], v[132:133], v[34:35], v[12:13] op_sel_hi:[0,1,1]
	v_pk_fma_f32 v[14:15], v[132:133], v[42:43], v[14:15] op_sel_hi:[0,1,1]
	v_pk_fma_f32 v[16:17], v[132:133], v[50:51], v[16:17] op_sel_hi:[0,1,1]
	v_fmac_f32_e32 v23, v132, v59
	s_cmp_eq_u32 s6, 3
	s_cbranch_scc0 .Lada_more
	v_readfirstlane_b32 s100, v8
	v_readfirstlane_b32 s101, v9
	s_nop 4
.Lada_more:
	global_load_dword v70, v200, s[100:101]
	s_add_u32 s100, s100, 0x6000
	s_addc_u32 s101, s101, 0
	global_load_dword v72, v200, s[100:101]
	s_add_u32 s100, s100, 0x6000
	s_addc_u32 s101, s101, 0
	global_load_dword v74, v200, s[100:101]
	s_add_u32 s100, s100, 0x6000
	s_addc_u32 s101, s101, 0
	global_load_dword v76, v200, s[100:101]
	s_add_u32 s100, s100, 0x6000
	s_addc_u32 s101, s101, 0
	global_load_dword v78, v200, s[100:101]
	s_add_u32 s100, s100, 0x6000
	s_addc_u32 s101, s101, 0
	global_load_dword v80, v200, s[100:101]
	s_add_u32 s100, s100, 0x6000
	s_addc_u32 s101, s101, 0
	global_load_dword v82, v200, s[100:101]
	s_add_u32 s100, s100, 0x6000
	s_addc_u32 s101, s101, 0
	global_load_dword v84, v200, s[100:101]
	s_add_u32 s100, s100, 0x6000
	s_addc_u32 s101, s101, 0
	global_load_dword v86, v200, s[100:101]
	s_add_u32 s100, s100, 0x6000
	s_addc_u32 s101, s101, 0
	global_load_dword v88, v200, s[100:101]
	s_add_u32 s100, s100, 0x6000
	s_addc_u32 s101, s101, 0
	global_load_dword v90, v200, s[100:101]
	s_add_u32 s100, s100, 0x6000
	s_addc_u32 s101, s101, 0
	global_load_dword v92, v200, s[100:101]
	s_add_u32 s100, s100, 0x6000
	s_addc_u32 s101, s101, 0
	global_load_dword v94, v200, s[100:101]
	s_add_u32 s100, s100, 0x6000
	s_addc_u32 s101, s101, 0
	global_load_dword v96, v200, s[100:101]
	s_add_u32 s100, s100, 0x6000
	s_addc_u32 s101, s101, 0
	global_load_dword v98, v200, s[100:101]
	s_add_u32 s100, s100, 0x6000
	s_addc_u32 s101, s101, 0
	global_load_dword v100, v200, s[100:101]
	s_add_u32 s100, s100, 0x6000
	s_addc_u32 s101, s101, 0
	global_load_dword v102, v200, s[100:101]
	s_add_u32 s100, s100, 0x6000
	s_addc_u32 s101, s101, 0
	global_load_dword v104, v200, s[100:101]
	s_add_u32 s100, s100, 0x6000
	s_addc_u32 s101, s101, 0
	global_load_dword v106, v200, s[100:101]
	s_add_u32 s100, s100, 0x6000
	s_addc_u32 s101, s101, 0
	global_load_dword v108, v200, s[100:101]
	s_add_u32 s100, s100, 0x6000
	s_addc_u32 s101, s101, 0
	global_load_dword v110, v200, s[100:101]
	s_add_u32 s100, s100, 0x6000
	s_addc_u32 s101, s101, 0
	global_load_dword v112, v200, s[100:101]
	s_add_u32 s100, s100, 0x6000
	s_addc_u32 s101, s101, 0
	global_load_dword v114, v200, s[100:101]
	s_add_u32 s100, s100, 0x6000
	s_addc_u32 s101, s101, 0
	global_load_dword v116, v200, s[100:101]
	s_add_u32 s100, s100, 0x6000
	s_addc_u32 s101, s101, 0
	global_load_dword v118, v200, s[100:101]
	s_add_u32 s100, s100, 0x6000
	s_addc_u32 s101, s101, 0
	global_load_dword v120, v200, s[100:101]
	s_add_u32 s100, s100, 0x6000
	s_addc_u32 s101, s101, 0
	global_load_dword v122, v200, s[100:101]
	s_add_u32 s100, s100, 0x6000
	s_addc_u32 s101, s101, 0
	global_load_dword v124, v200, s[100:101]
	s_add_u32 s100, s100, 0x6000
	s_addc_u32 s101, s101, 0
	global_load_dword v126, v200, s[100:101]
	s_add_u32 s100, s100, 0x6000
	s_addc_u32 s101, s101, 0
	global_load_dword v128, v200, s[100:101]
	s_add_u32 s100, s100, 0x6000
	s_addc_u32 s101, s101, 0
	global_load_dword v130, v200, s[100:101]
	s_add_u32 s100, s100, 0x6000
	s_addc_u32 s101, s101, 0
	global_load_dword v132, v200, s[100:101]
	s_add_u32 s100, s100, 0x6000
	s_addc_u32 s101, s101, 0
	ds_read_b128 v[24:27], v22 offset:4096
	ds_read_b128 v[28:31], v22 offset:8192
	ds_read_b128 v[32:35], v22 offset:12288
	ds_read_b128 v[36:39], v22 offset:16384
	ds_read_b128 v[40:43], v22 offset:20480
	ds_read_b128 v[44:47], v22 offset:24576
	ds_read_b128 v[48:51], v22 offset:28672
	ds_read_b128 v[52:55], v22
	ds_read_b128 v[56:59], v22 offset:32768
	s_waitcnt lgkmcnt(8)
	v_mov_b32_e32 v69, v24
	v_add_u32_e32 v22, 16, v22
	s_waitcnt lgkmcnt(1)
	v_mov_b32_e32 v68, v52
	v_mov_b32_e32 v24, v53
	v_mov_b32_e32 v52, v54
	v_mov_b32_e32 v53, v26
	v_mov_b32_e32 v26, v55
	v_mov_b32_e32 v54, v28
	v_mov_b32_e32 v55, v32
	v_mov_b32_e32 v32, v29
	v_mov_b32_e32 v28, v30
	v_mov_b32_e32 v29, v34
	v_mov_b32_e32 v34, v31
	v_mov_b32_e32 v30, v36
	v_mov_b32_e32 v31, v40
	v_mov_b32_e32 v40, v37
	v_mov_b32_e32 v36, v38
	v_mov_b32_e32 v37, v42
	v_mov_b32_e32 v42, v39
	v_mov_b32_e32 v38, v44
	v_mov_b32_e32 v39, v48
	v_mov_b32_e32 v48, v45
	v_mov_b32_e32 v44, v46
	v_mov_b32_e32 v45, v50
	v_mov_b32_e32 v50, v47
	s_waitcnt vmcnt(60)
	v_pk_fma_f32 v[10:11], v[134:135], v[68:69], v[10:11] op_sel_hi:[0,1,1]
	v_pk_fma_f32 v[12:13], v[134:135], v[54:55], v[12:13] op_sel_hi:[0,1,1]
	v_pk_fma_f32 v[14:15], v[134:135], v[30:31], v[14:15] op_sel_hi:[0,1,1]
	v_pk_fma_f32 v[16:17], v[134:135], v[38:39], v[16:17] op_sel_hi:[0,1,1]
	s_waitcnt lgkmcnt(0)
	v_fmac_f32_e32 v23, v134, v56
	v_pk_fma_f32 v[10:11], v[136:137], v[24:25], v[10:11] op_sel_hi:[0,1,1]
	v_pk_fma_f32 v[12:13], v[136:137], v[32:33], v[12:13] op_sel_hi:[0,1,1]
	v_pk_fma_f32 v[14:15], v[136:137], v[40:41], v[14:15] op_sel_hi:[0,1,1]
	v_pk_fma_f32 v[16:17], v[136:137], v[48:49], v[16:17] op_sel_hi:[0,1,1]
	v_fmac_f32_e32 v23, v136, v57
	v_pk_fma_f32 v[10:11], v[138:139], v[52:53], v[10:11] op_sel_hi:[0,1,1]
	v_pk_fma_f32 v[12:13], v[138:139], v[28:29], v[12:13] op_sel_hi:[0,1,1]
	v_pk_fma_f32 v[14:15], v[138:139], v[36:37], v[14:15] op_sel_hi:[0,1,1]
	v_pk_fma_f32 v[16:17], v[138:139], v[44:45], v[16:17] op_sel_hi:[0,1,1]
	v_fmac_f32_e32 v23, v138, v58
	v_pk_fma_f32 v[10:11], v[140:141], v[26:27], v[10:11] op_sel_hi:[0,1,1]
	v_pk_fma_f32 v[12:13], v[140:141], v[34:35], v[12:13] op_sel_hi:[0,1,1]
	v_pk_fma_f32 v[14:15], v[140:141], v[42:43], v[14:15] op_sel_hi:[0,1,1]
	v_pk_fma_f32 v[16:17], v[140:141], v[50:51], v[16:17] op_sel_hi:[0,1,1]
	v_fmac_f32_e32 v23, v140, v59
	ds_read_b128 v[24:27], v22 offset:4096
	ds_read_b128 v[28:31], v22 offset:8192
	ds_read_b128 v[32:35], v22 offset:12288
	ds_read_b128 v[36:39], v22 offset:16384
	ds_read_b128 v[40:43], v22 offset:20480
	ds_read_b128 v[44:47], v22 offset:24576
	ds_read_b128 v[48:51], v22 offset:28672
	ds_read_b128 v[52:55], v22
	ds_read_b128 v[56:59], v22 offset:32768
	s_waitcnt lgkmcnt(8)
	v_mov_b32_e32 v69, v24
	v_add_u32_e32 v22, 16, v22
	s_waitcnt lgkmcnt(1)
	v_mov_b32_e32 v68, v52
	v_mov_b32_e32 v24, v53
	v_mov_b32_e32 v52, v54
	v_mov_b32_e32 v53, v26
	v_mov_b32_e32 v26, v55
	v_mov_b32_e32 v54, v28
	v_mov_b32_e32 v55, v32
	v_mov_b32_e32 v32, v29
	v_mov_b32_e32 v28, v30
	v_mov_b32_e32 v29, v34
	v_mov_b32_e32 v34, v31
	v_mov_b32_e32 v30, v36
	v_mov_b32_e32 v31, v40
	v_mov_b32_e32 v40, v37
	v_mov_b32_e32 v36, v38
	v_mov_b32_e32 v37, v42
	v_mov_b32_e32 v42, v39
	v_mov_b32_e32 v38, v44
	v_mov_b32_e32 v39, v48
	v_mov_b32_e32 v48, v45
	v_mov_b32_e32 v44, v46
	v_mov_b32_e32 v45, v50
	v_mov_b32_e32 v50, v47
	s_waitcnt vmcnt(56)
	v_pk_fma_f32 v[10:11], v[142:143], v[68:69], v[10:11] op_sel_hi:[0,1,1]
	v_pk_fma_f32 v[12:13], v[142:143], v[54:55], v[12:13] op_sel_hi:[0,1,1]
	v_pk_fma_f32 v[14:15], v[142:143], v[30:31], v[14:15] op_sel_hi:[0,1,1]
	v_pk_fma_f32 v[16:17], v[142:143], v[38:39], v[16:17] op_sel_hi:[0,1,1]
	s_waitcnt lgkmcnt(0)
	v_fmac_f32_e32 v23, v142, v56
	v_pk_fma_f32 v[10:11], v[144:145], v[24:25], v[10:11] op_sel_hi:[0,1,1]
	v_pk_fma_f32 v[12:13], v[144:145], v[32:33], v[12:13] op_sel_hi:[0,1,1]
	v_pk_fma_f32 v[14:15], v[144:145], v[40:41], v[14:15] op_sel_hi:[0,1,1]
	v_pk_fma_f32 v[16:17], v[144:145], v[48:49], v[16:17] op_sel_hi:[0,1,1]
	v_fmac_f32_e32 v23, v144, v57
	v_pk_fma_f32 v[10:11], v[146:147], v[52:53], v[10:11] op_sel_hi:[0,1,1]
	v_pk_fma_f32 v[12:13], v[146:147], v[28:29], v[12:13] op_sel_hi:[0,1,1]
	v_pk_fma_f32 v[14:15], v[146:147], v[36:37], v[14:15] op_sel_hi:[0,1,1]
	v_pk_fma_f32 v[16:17], v[146:147], v[44:45], v[16:17] op_sel_hi:[0,1,1]
	v_fmac_f32_e32 v23, v146, v58
	v_pk_fma_f32 v[10:11], v[148:149], v[26:27], v[10:11] op_sel_hi:[0,1,1]
	v_pk_fma_f32 v[12:13], v[148:149], v[34:35], v[12:13] op_sel_hi:[0,1,1]
	v_pk_fma_f32 v[14:15], v[148:149], v[42:43], v[14:15] op_sel_hi:[0,1,1]
	v_pk_fma_f32 v[16:17], v[148:149], v[50:51], v[16:17] op_sel_hi:[0,1,1]
	v_fmac_f32_e32 v23, v148, v59
	ds_read_b128 v[24:27], v22 offset:4096
	ds_read_b128 v[28:31], v22 offset:8192
	ds_read_b128 v[32:35], v22 offset:12288
	ds_read_b128 v[36:39], v22 offset:16384
	ds_read_b128 v[40:43], v22 offset:20480
	ds_read_b128 v[44:47], v22 offset:24576
	ds_read_b128 v[48:51], v22 offset:28672
	ds_read_b128 v[52:55], v22
	ds_read_b128 v[56:59], v22 offset:32768
	s_waitcnt lgkmcnt(8)
	v_mov_b32_e32 v69, v24
	v_add_u32_e32 v22, 16, v22
	s_waitcnt lgkmcnt(1)
	v_mov_b32_e32 v68, v52
	v_mov_b32_e32 v24, v53
	v_mov_b32_e32 v52, v54
	v_mov_b32_e32 v53, v26
	v_mov_b32_e32 v26, v55
	v_mov_b32_e32 v54, v28
	v_mov_b32_e32 v55, v32
	v_mov_b32_e32 v32, v29
	v_mov_b32_e32 v28, v30
	v_mov_b32_e32 v29, v34
	v_mov_b32_e32 v34, v31
	v_mov_b32_e32 v30, v36
	v_mov_b32_e32 v31, v40
	v_mov_b32_e32 v40, v37
	v_mov_b32_e32 v36, v38
	v_mov_b32_e32 v37, v42
	v_mov_b32_e32 v42, v39
	v_mov_b32_e32 v38, v44
	v_mov_b32_e32 v39, v48
	v_mov_b32_e32 v48, v45
	v_mov_b32_e32 v44, v46
	v_mov_b32_e32 v45, v50
	v_mov_b32_e32 v50, v47
	s_waitcnt vmcnt(52)
	v_pk_fma_f32 v[10:11], v[150:151], v[68:69], v[10:11] op_sel_hi:[0,1,1]
	v_pk_fma_f32 v[12:13], v[150:151], v[54:55], v[12:13] op_sel_hi:[0,1,1]
	v_pk_fma_f32 v[14:15], v[150:151], v[30:31], v[14:15] op_sel_hi:[0,1,1]
	v_pk_fma_f32 v[16:17], v[150:151], v[38:39], v[16:17] op_sel_hi:[0,1,1]
	s_waitcnt lgkmcnt(0)
	v_fmac_f32_e32 v23, v150, v56
	v_pk_fma_f32 v[10:11], v[152:153], v[24:25], v[10:11] op_sel_hi:[0,1,1]
	v_pk_fma_f32 v[12:13], v[152:153], v[32:33], v[12:13] op_sel_hi:[0,1,1]
	v_pk_fma_f32 v[14:15], v[152:153], v[40:41], v[14:15] op_sel_hi:[0,1,1]
	v_pk_fma_f32 v[16:17], v[152:153], v[48:49], v[16:17] op_sel_hi:[0,1,1]
	v_fmac_f32_e32 v23, v152, v57
	v_pk_fma_f32 v[10:11], v[154:155], v[52:53], v[10:11] op_sel_hi:[0,1,1]
	v_pk_fma_f32 v[12:13], v[154:155], v[28:29], v[12:13] op_sel_hi:[0,1,1]
	v_pk_fma_f32 v[14:15], v[154:155], v[36:37], v[14:15] op_sel_hi:[0,1,1]
	v_pk_fma_f32 v[16:17], v[154:155], v[44:45], v[16:17] op_sel_hi:[0,1,1]
	v_fmac_f32_e32 v23, v154, v58
	v_pk_fma_f32 v[10:11], v[156:157], v[26:27], v[10:11] op_sel_hi:[0,1,1]
	v_pk_fma_f32 v[12:13], v[156:157], v[34:35], v[12:13] op_sel_hi:[0,1,1]
	v_pk_fma_f32 v[14:15], v[156:157], v[42:43], v[14:15] op_sel_hi:[0,1,1]
	v_pk_fma_f32 v[16:17], v[156:157], v[50:51], v[16:17] op_sel_hi:[0,1,1]
	v_fmac_f32_e32 v23, v156, v59
	ds_read_b128 v[24:27], v22 offset:4096
	ds_read_b128 v[28:31], v22 offset:8192
	ds_read_b128 v[32:35], v22 offset:12288
	ds_read_b128 v[36:39], v22 offset:16384
	ds_read_b128 v[40:43], v22 offset:20480
	ds_read_b128 v[44:47], v22 offset:24576
	ds_read_b128 v[48:51], v22 offset:28672
	ds_read_b128 v[52:55], v22
	ds_read_b128 v[56:59], v22 offset:32768
	s_waitcnt lgkmcnt(8)
	v_mov_b32_e32 v69, v24
	v_add_u32_e32 v22, 16, v22
	s_waitcnt lgkmcnt(1)
	v_mov_b32_e32 v68, v52
	v_mov_b32_e32 v24, v53
	v_mov_b32_e32 v52, v54
	v_mov_b32_e32 v53, v26
	v_mov_b32_e32 v26, v55
	v_mov_b32_e32 v54, v28
	v_mov_b32_e32 v55, v32
	v_mov_b32_e32 v32, v29
	v_mov_b32_e32 v28, v30
	v_mov_b32_e32 v29, v34
	v_mov_b32_e32 v34, v31
	v_mov_b32_e32 v30, v36
	v_mov_b32_e32 v31, v40
	v_mov_b32_e32 v40, v37
	v_mov_b32_e32 v36, v38
	v_mov_b32_e32 v37, v42
	v_mov_b32_e32 v42, v39
	v_mov_b32_e32 v38, v44
	v_mov_b32_e32 v39, v48
	v_mov_b32_e32 v48, v45
	v_mov_b32_e32 v44, v46
	v_mov_b32_e32 v45, v50
	v_mov_b32_e32 v50, v47
	s_waitcnt vmcnt(48)
	v_pk_fma_f32 v[10:11], v[158:159], v[68:69], v[10:11] op_sel_hi:[0,1,1]
	v_pk_fma_f32 v[12:13], v[158:159], v[54:55], v[12:13] op_sel_hi:[0,1,1]
	v_pk_fma_f32 v[14:15], v[158:159], v[30:31], v[14:15] op_sel_hi:[0,1,1]
	v_pk_fma_f32 v[16:17], v[158:159], v[38:39], v[16:17] op_sel_hi:[0,1,1]
	s_waitcnt lgkmcnt(0)
	v_fmac_f32_e32 v23, v158, v56
	v_pk_fma_f32 v[10:11], v[160:161], v[24:25], v[10:11] op_sel_hi:[0,1,1]
	v_pk_fma_f32 v[12:13], v[160:161], v[32:33], v[12:13] op_sel_hi:[0,1,1]
	v_pk_fma_f32 v[14:15], v[160:161], v[40:41], v[14:15] op_sel_hi:[0,1,1]
	v_pk_fma_f32 v[16:17], v[160:161], v[48:49], v[16:17] op_sel_hi:[0,1,1]
	v_fmac_f32_e32 v23, v160, v57
	v_pk_fma_f32 v[10:11], v[162:163], v[52:53], v[10:11] op_sel_hi:[0,1,1]
	v_pk_fma_f32 v[12:13], v[162:163], v[28:29], v[12:13] op_sel_hi:[0,1,1]
	v_pk_fma_f32 v[14:15], v[162:163], v[36:37], v[14:15] op_sel_hi:[0,1,1]
	v_pk_fma_f32 v[16:17], v[162:163], v[44:45], v[16:17] op_sel_hi:[0,1,1]
	v_fmac_f32_e32 v23, v162, v58
	v_pk_fma_f32 v[10:11], v[164:165], v[26:27], v[10:11] op_sel_hi:[0,1,1]
	v_pk_fma_f32 v[12:13], v[164:165], v[34:35], v[12:13] op_sel_hi:[0,1,1]
	v_pk_fma_f32 v[14:15], v[164:165], v[42:43], v[14:15] op_sel_hi:[0,1,1]
	v_pk_fma_f32 v[16:17], v[164:165], v[50:51], v[16:17] op_sel_hi:[0,1,1]
	v_fmac_f32_e32 v23, v164, v59
	ds_read_b128 v[24:27], v22 offset:4096
	ds_read_b128 v[28:31], v22 offset:8192
	ds_read_b128 v[32:35], v22 offset:12288
	ds_read_b128 v[36:39], v22 offset:16384
	ds_read_b128 v[40:43], v22 offset:20480
	ds_read_b128 v[44:47], v22 offset:24576
	ds_read_b128 v[48:51], v22 offset:28672
	ds_read_b128 v[52:55], v22
	ds_read_b128 v[56:59], v22 offset:32768
	s_waitcnt lgkmcnt(8)
	v_mov_b32_e32 v69, v24
	v_add_u32_e32 v22, 16, v22
	s_waitcnt lgkmcnt(1)
	v_mov_b32_e32 v68, v52
	v_mov_b32_e32 v24, v53
	v_mov_b32_e32 v52, v54
	v_mov_b32_e32 v53, v26
	v_mov_b32_e32 v26, v55
	v_mov_b32_e32 v54, v28
	v_mov_b32_e32 v55, v32
	v_mov_b32_e32 v32, v29
	v_mov_b32_e32 v28, v30
	v_mov_b32_e32 v29, v34
	v_mov_b32_e32 v34, v31
	v_mov_b32_e32 v30, v36
	v_mov_b32_e32 v31, v40
	v_mov_b32_e32 v40, v37
	v_mov_b32_e32 v36, v38
	v_mov_b32_e32 v37, v42
	v_mov_b32_e32 v42, v39
	v_mov_b32_e32 v38, v44
	v_mov_b32_e32 v39, v48
	v_mov_b32_e32 v48, v45
	v_mov_b32_e32 v44, v46
	v_mov_b32_e32 v45, v50
	v_mov_b32_e32 v50, v47
	s_waitcnt vmcnt(44)
	v_pk_fma_f32 v[10:11], v[166:167], v[68:69], v[10:11] op_sel_hi:[0,1,1]
	v_pk_fma_f32 v[12:13], v[166:167], v[54:55], v[12:13] op_sel_hi:[0,1,1]
	v_pk_fma_f32 v[14:15], v[166:167], v[30:31], v[14:15] op_sel_hi:[0,1,1]
	v_pk_fma_f32 v[16:17], v[166:167], v[38:39], v[16:17] op_sel_hi:[0,1,1]
	s_waitcnt lgkmcnt(0)
	v_fmac_f32_e32 v23, v166, v56
	v_pk_fma_f32 v[10:11], v[168:169], v[24:25], v[10:11] op_sel_hi:[0,1,1]
	v_pk_fma_f32 v[12:13], v[168:169], v[32:33], v[12:13] op_sel_hi:[0,1,1]
	v_pk_fma_f32 v[14:15], v[168:169], v[40:41], v[14:15] op_sel_hi:[0,1,1]
	v_pk_fma_f32 v[16:17], v[168:169], v[48:49], v[16:17] op_sel_hi:[0,1,1]
	v_fmac_f32_e32 v23, v168, v57
	v_pk_fma_f32 v[10:11], v[170:171], v[52:53], v[10:11] op_sel_hi:[0,1,1]
	v_pk_fma_f32 v[12:13], v[170:171], v[28:29], v[12:13] op_sel_hi:[0,1,1]
	v_pk_fma_f32 v[14:15], v[170:171], v[36:37], v[14:15] op_sel_hi:[0,1,1]
	v_pk_fma_f32 v[16:17], v[170:171], v[44:45], v[16:17] op_sel_hi:[0,1,1]
	v_fmac_f32_e32 v23, v170, v58
	v_pk_fma_f32 v[10:11], v[172:173], v[26:27], v[10:11] op_sel_hi:[0,1,1]
	v_pk_fma_f32 v[12:13], v[172:173], v[34:35], v[12:13] op_sel_hi:[0,1,1]
	v_pk_fma_f32 v[14:15], v[172:173], v[42:43], v[14:15] op_sel_hi:[0,1,1]
	v_pk_fma_f32 v[16:17], v[172:173], v[50:51], v[16:17] op_sel_hi:[0,1,1]
	v_fmac_f32_e32 v23, v172, v59
	ds_read_b128 v[24:27], v22 offset:4096
	ds_read_b128 v[28:31], v22 offset:8192
	ds_read_b128 v[32:35], v22 offset:12288
	ds_read_b128 v[36:39], v22 offset:16384
	ds_read_b128 v[40:43], v22 offset:20480
	ds_read_b128 v[44:47], v22 offset:24576
	ds_read_b128 v[48:51], v22 offset:28672
	ds_read_b128 v[52:55], v22
	ds_read_b128 v[56:59], v22 offset:32768
	s_waitcnt lgkmcnt(8)
	v_mov_b32_e32 v69, v24
	v_add_u32_e32 v22, 16, v22
	s_waitcnt lgkmcnt(1)
	v_mov_b32_e32 v68, v52
	v_mov_b32_e32 v24, v53
	v_mov_b32_e32 v52, v54
	v_mov_b32_e32 v53, v26
	v_mov_b32_e32 v26, v55
	v_mov_b32_e32 v54, v28
	v_mov_b32_e32 v55, v32
	v_mov_b32_e32 v32, v29
	v_mov_b32_e32 v28, v30
	v_mov_b32_e32 v29, v34
	v_mov_b32_e32 v34, v31
	v_mov_b32_e32 v30, v36
	v_mov_b32_e32 v31, v40
	v_mov_b32_e32 v40, v37
	v_mov_b32_e32 v36, v38
	v_mov_b32_e32 v37, v42
	v_mov_b32_e32 v42, v39
	v_mov_b32_e32 v38, v44
	v_mov_b32_e32 v39, v48
	v_mov_b32_e32 v48, v45
	v_mov_b32_e32 v44, v46
	v_mov_b32_e32 v45, v50
	v_mov_b32_e32 v50, v47
	s_waitcnt vmcnt(40)
	v_pk_fma_f32 v[10:11], v[174:175], v[68:69], v[10:11] op_sel_hi:[0,1,1]
	v_pk_fma_f32 v[12:13], v[174:175], v[54:55], v[12:13] op_sel_hi:[0,1,1]
	v_pk_fma_f32 v[14:15], v[174:175], v[30:31], v[14:15] op_sel_hi:[0,1,1]
	v_pk_fma_f32 v[16:17], v[174:175], v[38:39], v[16:17] op_sel_hi:[0,1,1]
	s_waitcnt lgkmcnt(0)
	v_fmac_f32_e32 v23, v174, v56
	v_pk_fma_f32 v[10:11], v[176:177], v[24:25], v[10:11] op_sel_hi:[0,1,1]
	v_pk_fma_f32 v[12:13], v[176:177], v[32:33], v[12:13] op_sel_hi:[0,1,1]
	v_pk_fma_f32 v[14:15], v[176:177], v[40:41], v[14:15] op_sel_hi:[0,1,1]
	v_pk_fma_f32 v[16:17], v[176:177], v[48:49], v[16:17] op_sel_hi:[0,1,1]
	v_fmac_f32_e32 v23, v176, v57
	v_pk_fma_f32 v[10:11], v[178:179], v[52:53], v[10:11] op_sel_hi:[0,1,1]
	v_pk_fma_f32 v[12:13], v[178:179], v[28:29], v[12:13] op_sel_hi:[0,1,1]
	v_pk_fma_f32 v[14:15], v[178:179], v[36:37], v[14:15] op_sel_hi:[0,1,1]
	v_pk_fma_f32 v[16:17], v[178:179], v[44:45], v[16:17] op_sel_hi:[0,1,1]
	v_fmac_f32_e32 v23, v178, v58
	v_pk_fma_f32 v[10:11], v[180:181], v[26:27], v[10:11] op_sel_hi:[0,1,1]
	v_pk_fma_f32 v[12:13], v[180:181], v[34:35], v[12:13] op_sel_hi:[0,1,1]
	v_pk_fma_f32 v[14:15], v[180:181], v[42:43], v[14:15] op_sel_hi:[0,1,1]
	v_pk_fma_f32 v[16:17], v[180:181], v[50:51], v[16:17] op_sel_hi:[0,1,1]
	v_fmac_f32_e32 v23, v180, v59
	ds_read_b128 v[24:27], v22 offset:4096
	ds_read_b128 v[28:31], v22 offset:8192
	ds_read_b128 v[32:35], v22 offset:12288
	ds_read_b128 v[36:39], v22 offset:16384
	ds_read_b128 v[40:43], v22 offset:20480
	ds_read_b128 v[44:47], v22 offset:24576
	ds_read_b128 v[48:51], v22 offset:28672
	ds_read_b128 v[52:55], v22
	ds_read_b128 v[56:59], v22 offset:32768
	s_waitcnt lgkmcnt(8)
	v_mov_b32_e32 v69, v24
	v_add_u32_e32 v22, 16, v22
	s_waitcnt lgkmcnt(1)
	v_mov_b32_e32 v68, v52
	v_mov_b32_e32 v24, v53
	v_mov_b32_e32 v52, v54
	v_mov_b32_e32 v53, v26
	v_mov_b32_e32 v26, v55
	v_mov_b32_e32 v54, v28
	v_mov_b32_e32 v55, v32
	v_mov_b32_e32 v32, v29
	v_mov_b32_e32 v28, v30
	v_mov_b32_e32 v29, v34
	v_mov_b32_e32 v34, v31
	v_mov_b32_e32 v30, v36
	v_mov_b32_e32 v31, v40
	v_mov_b32_e32 v40, v37
	v_mov_b32_e32 v36, v38
	v_mov_b32_e32 v37, v42
	v_mov_b32_e32 v42, v39
	v_mov_b32_e32 v38, v44
	v_mov_b32_e32 v39, v48
	v_mov_b32_e32 v48, v45
	v_mov_b32_e32 v44, v46
	v_mov_b32_e32 v45, v50
	v_mov_b32_e32 v50, v47
	s_waitcnt vmcnt(36)
	v_pk_fma_f32 v[10:11], v[182:183], v[68:69], v[10:11] op_sel_hi:[0,1,1]
	v_pk_fma_f32 v[12:13], v[182:183], v[54:55], v[12:13] op_sel_hi:[0,1,1]
	v_pk_fma_f32 v[14:15], v[182:183], v[30:31], v[14:15] op_sel_hi:[0,1,1]
	v_pk_fma_f32 v[16:17], v[182:183], v[38:39], v[16:17] op_sel_hi:[0,1,1]
	s_waitcnt lgkmcnt(0)
	v_fmac_f32_e32 v23, v182, v56
	v_pk_fma_f32 v[10:11], v[184:185], v[24:25], v[10:11] op_sel_hi:[0,1,1]
	v_pk_fma_f32 v[12:13], v[184:185], v[32:33], v[12:13] op_sel_hi:[0,1,1]
	v_pk_fma_f32 v[14:15], v[184:185], v[40:41], v[14:15] op_sel_hi:[0,1,1]
	v_pk_fma_f32 v[16:17], v[184:185], v[48:49], v[16:17] op_sel_hi:[0,1,1]
	v_fmac_f32_e32 v23, v184, v57
	v_pk_fma_f32 v[10:11], v[186:187], v[52:53], v[10:11] op_sel_hi:[0,1,1]
	v_pk_fma_f32 v[12:13], v[186:187], v[28:29], v[12:13] op_sel_hi:[0,1,1]
	v_pk_fma_f32 v[14:15], v[186:187], v[36:37], v[14:15] op_sel_hi:[0,1,1]
	v_pk_fma_f32 v[16:17], v[186:187], v[44:45], v[16:17] op_sel_hi:[0,1,1]
	v_fmac_f32_e32 v23, v186, v58
	v_pk_fma_f32 v[10:11], v[188:189], v[26:27], v[10:11] op_sel_hi:[0,1,1]
	v_pk_fma_f32 v[12:13], v[188:189], v[34:35], v[12:13] op_sel_hi:[0,1,1]
	v_pk_fma_f32 v[14:15], v[188:189], v[42:43], v[14:15] op_sel_hi:[0,1,1]
	v_pk_fma_f32 v[16:17], v[188:189], v[50:51], v[16:17] op_sel_hi:[0,1,1]
	v_fmac_f32_e32 v23, v188, v59
	ds_read_b128 v[24:27], v22 offset:4096
	ds_read_b128 v[28:31], v22 offset:8192
	ds_read_b128 v[32:35], v22 offset:12288
	ds_read_b128 v[36:39], v22 offset:16384
	ds_read_b128 v[40:43], v22 offset:20480
	ds_read_b128 v[44:47], v22 offset:24576
	ds_read_b128 v[48:51], v22 offset:28672
	ds_read_b128 v[52:55], v22
	ds_read_b128 v[56:59], v22 offset:32768
	s_waitcnt lgkmcnt(8)
	v_mov_b32_e32 v69, v24
	v_add_u32_e32 v22, 16, v22
	s_waitcnt lgkmcnt(1)
	v_mov_b32_e32 v68, v52
	v_mov_b32_e32 v24, v53
	v_mov_b32_e32 v52, v54
	v_mov_b32_e32 v53, v26
	v_mov_b32_e32 v26, v55
	v_mov_b32_e32 v54, v28
	v_mov_b32_e32 v55, v32
	v_mov_b32_e32 v32, v29
	v_mov_b32_e32 v28, v30
	v_mov_b32_e32 v29, v34
	v_mov_b32_e32 v34, v31
	v_mov_b32_e32 v30, v36
	v_mov_b32_e32 v31, v40
	v_mov_b32_e32 v40, v37
	v_mov_b32_e32 v36, v38
	v_mov_b32_e32 v37, v42
	v_mov_b32_e32 v42, v39
	v_mov_b32_e32 v38, v44
	v_mov_b32_e32 v39, v48
	v_mov_b32_e32 v48, v45
	v_mov_b32_e32 v44, v46
	v_mov_b32_e32 v45, v50
	v_mov_b32_e32 v50, v47
	s_waitcnt vmcnt(32)
	v_pk_fma_f32 v[10:11], v[190:191], v[68:69], v[10:11] op_sel_hi:[0,1,1]
	v_pk_fma_f32 v[12:13], v[190:191], v[54:55], v[12:13] op_sel_hi:[0,1,1]
	v_pk_fma_f32 v[14:15], v[190:191], v[30:31], v[14:15] op_sel_hi:[0,1,1]
	v_pk_fma_f32 v[16:17], v[190:191], v[38:39], v[16:17] op_sel_hi:[0,1,1]
	s_waitcnt lgkmcnt(0)
	v_fmac_f32_e32 v23, v190, v56
	v_pk_fma_f32 v[10:11], v[192:193], v[24:25], v[10:11] op_sel_hi:[0,1,1]
	v_pk_fma_f32 v[12:13], v[192:193], v[32:33], v[12:13] op_sel_hi:[0,1,1]
	v_pk_fma_f32 v[14:15], v[192:193], v[40:41], v[14:15] op_sel_hi:[0,1,1]
	v_pk_fma_f32 v[16:17], v[192:193], v[48:49], v[16:17] op_sel_hi:[0,1,1]
	v_fmac_f32_e32 v23, v192, v57
	v_pk_fma_f32 v[10:11], v[194:195], v[52:53], v[10:11] op_sel_hi:[0,1,1]
	v_pk_fma_f32 v[12:13], v[194:195], v[28:29], v[12:13] op_sel_hi:[0,1,1]
	v_pk_fma_f32 v[14:15], v[194:195], v[36:37], v[14:15] op_sel_hi:[0,1,1]
	v_pk_fma_f32 v[16:17], v[194:195], v[44:45], v[16:17] op_sel_hi:[0,1,1]
	v_fmac_f32_e32 v23, v194, v58
	v_pk_fma_f32 v[10:11], v[196:197], v[26:27], v[10:11] op_sel_hi:[0,1,1]
	v_pk_fma_f32 v[12:13], v[196:197], v[34:35], v[12:13] op_sel_hi:[0,1,1]
	v_pk_fma_f32 v[14:15], v[196:197], v[42:43], v[14:15] op_sel_hi:[0,1,1]
	v_pk_fma_f32 v[16:17], v[196:197], v[50:51], v[16:17] op_sel_hi:[0,1,1]
	v_fmac_f32_e32 v23, v196, v59
	s_add_i32 s6, s6, 1
	s_cmp_lt_u32 s6, 4
	s_cbranch_scc1 .Lada_loop
	ds_write2st64_b32 v20, v10, v11 offset0:144 offset1:146
	ds_write2st64_b32 v20, v12, v13 offset0:148 offset1:150
	ds_write2st64_b32 v20, v14, v15 offset0:152 offset1:154
	ds_write2st64_b32 v20, v16, v17 offset0:156 offset1:158
	ds_write_b32 v20, v23 offset:40960
	s_waitcnt lgkmcnt(0)
	s_barrier
	s_and_saveexec_b64 s[6:7], s[2:3]
	s_cbranch_execz .LBB0_14
	v_readlane_b32 s16, v251, 1
	s_mul_i32 s15, s4, 0x6000
	v_readlane_b32 s26, v251, 11
	s_mul_hi_i32 s5, s4, 0x6000
	v_readlane_b32 s17, v251, 2
	v_readlane_b32 s27, v251, 12
	s_add_u32 s16, s26, s15
	s_addc_u32 s17, s27, s5
	v_lshlrev_b64 v[6:7], 2, v[6:7]
	v_lshl_add_u64 v[8:9], s[16:17], 0, v[6:7]
	global_load_dword v60, v[8:9], off
	v_lshl_add_u64 v[6:7], s[0:1], 0, v[6:7]
	v_mad_i64_i32 v[6:7], s[4:5], s4, v21, v[6:7]
	v_add_co_u32_e32 v48, vcc, s8, v6
	ds_read2st64_b32 v[8:9], v1 offset0:144 offset1:146
	ds_read2st64_b32 v[10:11], v1 offset0:160 offset1:162
	ds_read2st64_b32 v[12:13], v1 offset0:180 offset1:182
	ds_read2st64_b32 v[14:15], v1 offset0:196 offset1:198
	ds_read2st64_b32 v[16:17], v1 offset0:164 offset1:166
	ds_read2st64_b32 v[22:23], v1 offset0:200 offset1:202
	ds_read2st64_b32 v[24:25], v1 offset0:148 offset1:150
	ds_read2st64_b32 v[26:27], v1 offset0:184 offset1:186
	ds_read2st64_b32 v[28:29], v1 offset0:168 offset1:170
	ds_read2st64_b32 v[30:31], v1 offset0:204 offset1:206
	ds_read2st64_b32 v[32:33], v1 offset0:152 offset1:154
	ds_read2st64_b32 v[34:35], v1 offset0:188 offset1:190
	ds_read2st64_b32 v[36:37], v1 offset0:172 offset1:174
	ds_read2st64_b32 v[38:39], v1 offset0:208 offset1:210
	ds_read2st64_b32 v[40:41], v1 offset0:156 offset1:158
	ds_read2st64_b32 v[42:43], v1 offset0:192 offset1:194
	ds_read2st64_b32 v[44:45], v1 offset0:176 offset1:178
	ds_read2st64_b32 v[46:47], v1 offset0:212 offset1:214
	v_addc_co_u32_e32 v49, vcc, 0, v7, vcc
	v_add_co_u32_e32 v50, vcc, s9, v6
	s_waitcnt lgkmcnt(14)
	v_add_f32_e32 v8, v8, v11
	v_addc_co_u32_e32 v51, vcc, 0, v7, vcc
	v_add_co_u32_e32 v52, vcc, s10, v6
	s_waitcnt lgkmcnt(13)
	v_add_f32_e32 v9, v9, v16
	v_addc_co_u32_e32 v53, vcc, 0, v7, vcc
	v_add_co_u32_e32 v54, vcc, s11, v6
	s_waitcnt lgkmcnt(11)
	v_add_f32_e32 v11, v24, v17
	s_waitcnt lgkmcnt(9)
	v_add_f32_e32 v16, v25, v28
	s_waitcnt lgkmcnt(7)
	v_add_f32_e32 v17, v32, v29
	s_waitcnt lgkmcnt(5)
	v_add_f32_e32 v24, v33, v36
	v_add_f32_e32 v8, v8, v12
	v_addc_co_u32_e32 v55, vcc, 0, v7, vcc
	v_add_f32_e32 v9, v9, v13
	v_add_f32_e32 v11, v11, v26
	v_add_f32_e32 v12, v16, v27
	v_add_f32_e32 v13, v17, v34
	v_add_f32_e32 v16, v24, v35
	v_add_f32_e32 v8, v8, v15
	v_add_co_u32_e32 v56, vcc, s12, v6
	v_add_f32_e32 v9, v9, v22
	v_add_f32_e32 v11, v11, v23
	v_add_f32_e32 v12, v12, v30
	v_add_f32_e32 v13, v13, v31
	s_waitcnt lgkmcnt(4)
	v_add_f32_e32 v15, v16, v38
	v_addc_co_u32_e32 v57, vcc, 0, v7, vcc
	v_add_co_u32_e32 v58, vcc, s13, v6
	s_waitcnt lgkmcnt(3)
	v_add_f32_e32 v25, v40, v37
	v_addc_co_u32_e32 v59, vcc, 0, v7, vcc
	s_waitcnt lgkmcnt(2)
	v_add_f32_e32 v17, v25, v42
	v_add_f32_e32 v16, v17, v39
	v_readlane_b32 s18, v251, 3
	v_readlane_b32 s19, v251, 4
	v_readlane_b32 s20, v251, 5
	v_readlane_b32 s21, v251, 6
	v_readlane_b32 s22, v251, 7
	v_readlane_b32 s23, v251, 8
	v_readlane_b32 s24, v251, 9
	v_readlane_b32 s25, v251, 10
	v_readlane_b32 s28, v251, 13
	v_readlane_b32 s29, v251, 14
	v_readlane_b32 s30, v251, 15
	v_readlane_b32 s31, v251, 16
	s_waitcnt vmcnt(0)
	v_add_f32_e32 v8, v60, v8
	v_add_f32_e32 v9, v60, v9
	v_add_f32_e32 v11, v60, v11
	v_add_f32_e32 v12, v60, v12
	v_add_f32_e32 v13, v60, v13
	v_add_f32_e32 v15, v60, v15
	global_store_dword v[6:7], v8, off
	global_store_dword v[48:49], v9, off
	global_store_dword v[50:51], v11, off
	global_store_dword v[52:53], v12, off
	global_store_dword v[54:55], v13, off
	global_store_dword v[56:57], v15, off
	s_waitcnt lgkmcnt(1)
	v_add_f32_e32 v8, v41, v44
	v_add_f32_e32 v8, v8, v43
	s_waitcnt lgkmcnt(0)
	v_add_f32_e32 v8, v8, v46
	v_add_f32_e32 v11, v60, v8
	v_add_co_u32_e32 v8, vcc, 0x2a000, v6
	v_add_f32_e32 v16, v60, v16
	s_nop 0
	v_addc_co_u32_e32 v9, vcc, 0, v7, vcc
	global_store_dword v[8:9], v11, off
	v_add_f32_e32 v8, v10, v45
	v_add_f32_e32 v8, v8, v14
	v_add_f32_e32 v8, v8, v47
	v_add_co_u32_e32 v6, vcc, 0x30000, v6
	v_add_f32_e32 v8, v60, v8
	s_nop 0
	v_addc_co_u32_e32 v7, vcc, 0, v7, vcc
	global_store_dword v[58:59], v16, off
	global_store_dword v[6:7], v8, off
	s_branch .LBB0_14
